# qkv: cooperative L2 prefetch 2 slabs ahead (each block touches only its share of the lines its XCD tile-sharing group needs), vmcnt(1)
# baseline (speedup 1.0000x reference)
.LBB3_2:
	s_load_dwordx4 s[4:7], s[0:1], 0x10
	s_lshl_b32 s0, s2, 2
	s_and_b32 s23, s0, 24
	s_ashr_i32 s3, s2, 5
	s_and_b32 s0, s0, 4
	s_bfe_u32 s20, s2, 0x20003
	s_add_i32 s23, s23, s3
	s_or_b32 s0, s0, s20
	v_lshrrev_b32_e32 v8, 3, v0
	s_lshl_b32 s24, s0, 8
	v_lshrrev_b32_e32 v9, 4, v0
	v_lshl_or_b32 v2, s23, 7, v8
	s_lshl_b32 s22, s23, 6
	v_xor_b32_e32 v10, v9, v0
	v_or_b32_e32 v6, s24, v8
	v_ashrrev_i32_e32 v3, 31, v2
	v_lshlrev_b64 v[2:3], 12, v[2:3]
	v_or_b32_e32 v4, s22, v8
	v_lshlrev_b32_e32 v96, 12, v6
	v_mov_b32_e32 v97, 0
	v_lshlrev_b32_e32 v10, 4, v10
	s_waitcnt lgkmcnt(0)
	s_lshr_b32 s38, s2, 5
	s_lshl_b32 s38, s38, 5
	s_add_i32 s38, s38, s24
	s_bfe_u32 s39, s2, 0x20003
	s_mul_i32 s39, s39, 48
	s_mov_b64 s[40:41], 0x80
	v_and_b32_e32 v203, 63, v0
	v_lshrrev_b32_e32 v204, 6, v0
	v_add_u32_e32 v205, s38, v203
	v_add_u32_e32 v206, s39, v203
	v_subrev_u32_e32 v206, 32, v206
	v_and_b32_e32 v207, 15, v203
	v_add_u32_e32 v207, s39, v207
	v_add_u32_e32 v207, 32, v207
	v_mov_b32_e32 v208, s39
	v_cmp_eq_u32_e32 vcc, 1, v204
	s_nop 1
	v_cndmask_b32_e32 v208, v208, v207, vcc
	v_cmp_eq_u32_e32 vcc, 0, v204
	s_nop 1
	v_cndmask_b32_e32 v208, v208, v206, vcc
	s_lshl_b32 s42, s23, 7
	v_add_u32_e32 v206, s42, v208
	s_add_i32 s42, s22, 0xf80
	v_add_u32_e32 v207, s42, v208
	v_cmp_gt_u32_e32 vcc, 0x80, v208
	s_nop 1
	v_cndmask_b32_e32 v206, v207, v206, vcc
	v_lshlrev_b32_e32 v206, 12, v206
	v_lshlrev_b32_e32 v205, 12, v205
	v_mov_b32_e32 v207, 0
	v_mov_b32_e32 v209, 0
	v_mov_b32_e32 v208, v205
	v_lshl_add_u64 v[206:207], s[10:11], 0, v[206:207]
	v_lshl_add_u64 v[208:209], s[8:9], 0, v[208:209]
	v_cmp_gt_u32_e32 vcc, 32, v0
	s_nop 1
	v_cndmask_b32_e32 v200, v206, v208, vcc
	v_cndmask_b32_e32 v201, v207, v209, vcc
	v_lshl_add_u64 v[200:201], v[200:201], 0, s[40:41]
	v_lshl_add_u64 v[2:3], s[10:11], 0, v[2:3]
	v_add_u32_e32 v4, 0x1000, v4
	v_lshl_add_u64 v[6:7], s[8:9], 0, v[96:97]
	v_and_b32_e32 v96, 0x70, v10
	v_ashrrev_i32_e32 v5, 31, v4
	v_lshl_add_u64 v[98:99], v[2:3], 0, v[96:97]
	v_lshrrev_b32_e32 v2, 1, v0
	v_lshlrev_b64 v[4:5], 12, v[4:5]
	v_and_b32_e32 v110, 31, v0
	v_and_b32_e32 v114, 0xc0, v2
	v_bfe_u32 v112, v0, 6, 1
	v_lshrrev_b32_e32 v1, 5, v0
	v_lshl_add_u64 v[4:5], s[10:11], 0, v[4:5]
	v_bfe_u32 v113, v0, 5, 1
	v_bfe_u32 v3, v0, 1, 3
	v_or_b32_e32 v2, v114, v110
	v_bitop3_b32 v1, v1, v3, 1 bitop3:0x6c
	v_bitop3_b32 v10, v113, v3, 2 bitop3:0x36
	v_bitop3_b32 v11, v113, v3, 4 bitop3:0x36
	v_bitop3_b32 v12, v113, v3, 6 bitop3:0x36
	v_lshl_add_u64 v[100:101], v[6:7], 0, v[96:97]
	v_lshl_add_u64 v[102:103], v[4:5], 0, v[96:97]
	v_lshl_add_u32 v4, v2, 7, 0
	v_lshlrev_b32_e32 v2, 13, v112
	v_lshlrev_b32_e32 v3, 7, v110
	v_lshlrev_b32_e32 v111, 5, v112
	v_lshlrev_b32_e32 v7, 4, v0
	v_add3_u32 v5, 0, v2, v3
	v_or_b32_e32 v2, v111, v110
	s_add_i32 s0, 0, 0x10000
	v_add_u32_e32 v115, 0, v7
	v_lshl_add_u32 v6, v2, 7, s0
	v_readfirstlane_b32 s0, v115
	v_add_u32_e32 v116, 0x2000, v115
	s_mov_b32 m0, s0
	s_mov_b64 s[12:13], 0x40000
	v_readfirstlane_b32 s0, v116
	v_add_u32_e32 v117, 0x4000, v115
	global_load_lds_dwordx4 v[100:101], off
	v_lshl_add_u64 v[2:3], v[100:101], 0, s[12:13]
	s_mov_b32 m0, s0
	s_mov_b64 s[14:15], 0x80000
	v_readfirstlane_b32 s0, v117
	v_add_u32_e32 v118, 0x6000, v115
	global_load_lds_dwordx4 v[2:3], off
	v_lshl_add_u64 v[2:3], v[100:101], 0, s[14:15]
	s_mov_b32 m0, s0
	s_mov_b64 s[16:17], 0xc0000
	v_readfirstlane_b32 s0, v118
	v_add_u32_e32 v119, 0x8000, v115
	global_load_lds_dwordx4 v[2:3], off
	v_lshl_add_u64 v[2:3], v[100:101], 0, s[16:17]
	s_mov_b32 m0, s0
	v_readfirstlane_b32 s0, v119
	v_add_u32_e32 v120, 0xa000, v115
	global_load_lds_dwordx4 v[2:3], off
	s_mov_b32 m0, s0
	v_readfirstlane_b32 s0, v120
	v_add_u32_e32 v121, 0x10000, v115
	global_load_lds_dwordx4 v[98:99], off
	v_lshl_add_u64 v[2:3], v[98:99], 0, s[12:13]
	s_mov_b32 m0, s0
	v_readfirstlane_b32 s0, v121
	global_load_lds_dwordx4 v[2:3], off
	s_mov_b32 m0, s0
	s_add_i32 s0, 0, 0x12000
	global_load_lds_dwordx4 v[102:103], off
	global_load_dword v202, v[200:201], off
	v_lshl_add_u64 v[200:201], v[200:201], 0, s[40:41]
	v_add_u32_e32 v122, s0, v7
	s_bfe_u32 s0, s2, 0x20001
	s_lshl_b32 s18, s0, 9
	s_lshl_b32 s19, s3, 6
	v_bitop3_b32 v0, v9, 7, v0 bitop3:0x48
	s_add_i32 s19, s19, s18
	v_lshlrev_b32_e32 v1, 4, v1
	v_lshlrev_b32_e32 v2, 4, v10
	v_lshlrev_b32_e32 v3, 4, v11
	v_lshlrev_b32_e32 v7, 4, v12
	v_lshlrev_b32_e32 v96, 4, v0
	v_or_b32_e32 v0, s19, v8
	v_add_u32_e32 v123, v4, v1
	v_add_u32_e32 v124, v5, v1
	v_add_u32_e32 v125, v6, v1
	v_add_u32_e32 v126, v4, v2
	v_add_u32_e32 v127, v5, v2
	v_add_u32_e32 v128, v6, v2
	v_add_u32_e32 v129, v4, v3
	v_add_u32_e32 v130, v5, v3
	v_add_u32_e32 v131, v6, v3
	v_add_u32_e32 v132, v4, v7
	v_add_u32_e32 v133, v5, v7
	v_add_u32_e32 v134, v6, v7
	v_add_u32_e32 v10, 0x12000, v4
	v_add_u32_e32 v11, 0x1a000, v5
	v_add_u32_e32 v6, 0x12000, v6
	v_add_u32_e32 v4, 0x13000, v4
	v_add_u32_e32 v5, 0x1b000, v5
	v_add_u32_e32 v0, 0x1000, v0
	v_add_u32_e32 v135, v10, v1
	v_add_u32_e32 v136, v4, v1
	v_add_u32_e32 v137, v11, v1
	v_add_u32_e32 v138, v5, v1
	v_add_u32_e32 v139, v6, v1
	v_ashrrev_i32_e32 v1, 31, v0
	v_lshlrev_b64 v[0:1], 12, v[0:1]
	s_lshl_b32 s0, s0, 10
	s_lshl_b32 s3, s3, 7
	v_lshl_add_u64 v[0:1], s[10:11], 0, v[0:1]
	s_mov_b64 s[18:19], 0x80
	s_add_i32 s3, s3, s0
	v_lshl_add_u64 v[104:105], v[0:1], 0, s[18:19]
	v_or_b32_e32 v0, s3, v8
	v_ashrrev_i32_e32 v1, 31, v0
	v_lshlrev_b64 v[0:1], 12, v[0:1]
	v_lshl_add_u64 v[106:107], s[10:11], 0, v[0:1]
	s_and_b32 s0, s2, 1
	v_lshlrev_b32_e32 v0, 12, v8
	s_waitcnt vmcnt(1)
	v_lshl_or_b32 v0, s0, 22, v0
	v_lshl_or_b32 v0, s20, 20, v0
	v_mov_b32_e32 v1, v97
	s_mov_b32 s1, 0
	v_add_u32_e32 v140, v10, v2
	v_add_u32_e32 v141, v4, v2
	v_add_u32_e32 v142, v11, v2
	v_add_u32_e32 v143, v5, v2
	v_add_u32_e32 v144, v6, v2
	v_add_u32_e32 v145, v10, v3
	v_add_u32_e32 v146, v4, v3
	v_add_u32_e32 v147, v11, v3
	v_add_u32_e32 v148, v5, v3
	v_add_u32_e32 v149, v6, v3
	v_add_u32_e32 v150, v10, v7
	v_add_u32_e32 v151, v4, v7
	v_add_u32_e32 v152, v11, v7
	v_add_u32_e32 v153, v5, v7
	v_add_u32_e32 v154, v6, v7
	v_lshl_add_u64 v[108:109], s[8:9], 0, v[0:1]
	s_movk_i32 s25, 0x80
	s_mov_b64 s[2:3], 0x40080
	s_mov_b64 s[8:9], 0x80080
	s_mov_b64 s[10:11], 0xc0080
	s_mov_b64 s[20:21], 0x100
	s_mov_b32 s26, 0
	v_mov_b32_e32 v32, v97
	v_mov_b32_e32 v33, v97
	v_mov_b32_e32 v34, v97
	v_mov_b32_e32 v35, v97
	v_mov_b32_e32 v36, v97
	v_mov_b32_e32 v37, v97
	v_mov_b32_e32 v38, v97
	v_mov_b32_e32 v39, v97
	v_mov_b32_e32 v40, v97
	v_mov_b32_e32 v41, v97
	v_mov_b32_e32 v42, v97
	v_mov_b32_e32 v43, v97
	v_mov_b32_e32 v44, v97
	v_mov_b32_e32 v45, v97
	v_mov_b32_e32 v46, v97
	v_mov_b32_e32 v47, v97
	v_mov_b32_e32 v48, v97
	v_mov_b32_e32 v49, v97
	v_mov_b32_e32 v50, v97
	v_mov_b32_e32 v51, v97
	v_mov_b32_e32 v52, v97
	v_mov_b32_e32 v53, v97
	v_mov_b32_e32 v54, v97
	v_mov_b32_e32 v55, v97
	v_mov_b32_e32 v56, v97
	v_mov_b32_e32 v57, v97
	v_mov_b32_e32 v58, v97
	v_mov_b32_e32 v59, v97
	v_mov_b32_e32 v60, v97
	v_mov_b32_e32 v61, v97
	v_mov_b32_e32 v62, v97
	v_mov_b32_e32 v63, v97
	v_mov_b32_e32 v64, v97
	v_mov_b32_e32 v65, v97
	v_mov_b32_e32 v66, v97
	v_mov_b32_e32 v67, v97
	v_mov_b32_e32 v68, v97
	v_mov_b32_e32 v69, v97
	v_mov_b32_e32 v70, v97
	v_mov_b32_e32 v71, v97
	v_mov_b32_e32 v72, v97
	v_mov_b32_e32 v73, v97
	v_mov_b32_e32 v74, v97
	v_mov_b32_e32 v75, v97
	v_mov_b32_e32 v76, v97
	v_mov_b32_e32 v77, v97
	v_mov_b32_e32 v78, v97
	v_mov_b32_e32 v79, v97
	v_mov_b32_e32 v80, v97
	v_mov_b32_e32 v81, v97
	v_mov_b32_e32 v82, v97
	v_mov_b32_e32 v83, v97
	v_mov_b32_e32 v84, v97
	v_mov_b32_e32 v85, v97
	v_mov_b32_e32 v86, v97
	v_mov_b32_e32 v87, v97
	v_mov_b32_e32 v88, v97
	v_mov_b32_e32 v89, v97
	v_mov_b32_e32 v90, v97
	v_mov_b32_e32 v91, v97
	v_mov_b32_e32 v92, v97
	v_mov_b32_e32 v93, v97
	v_mov_b32_e32 v94, v97
	v_mov_b32_e32 v95, v97
	v_mov_b32_e32 v16, v97
	v_mov_b32_e32 v17, v97
	v_mov_b32_e32 v18, v97
	v_mov_b32_e32 v19, v97
	v_mov_b32_e32 v20, v97
	v_mov_b32_e32 v21, v97
	v_mov_b32_e32 v22, v97
	v_mov_b32_e32 v23, v97
	v_mov_b32_e32 v24, v97
	v_mov_b32_e32 v25, v97
	v_mov_b32_e32 v26, v97
	v_mov_b32_e32 v27, v97
	v_mov_b32_e32 v28, v97
	v_mov_b32_e32 v29, v97
	v_mov_b32_e32 v30, v97
	v_mov_b32_e32 v31, v97
	v_mov_b32_e32 v0, v97
	v_mov_b32_e32 v2, v97
	v_mov_b32_e32 v3, v97
	v_mov_b32_e32 v4, v97
	v_mov_b32_e32 v5, v97
	v_mov_b32_e32 v6, v97
	v_mov_b32_e32 v7, v97
	v_mov_b32_e32 v8, v97
	v_mov_b32_e32 v9, v97
	v_mov_b32_e32 v10, v97
	v_mov_b32_e32 v11, v97
	v_mov_b32_e32 v12, v97
	v_mov_b32_e32 v13, v97
	v_mov_b32_e32 v14, v97
	v_mov_b32_e32 v15, v97
	v_add_u32_e32 v155, 0x10000, v122
	s_waitcnt vmcnt(1) lgkmcnt(0)
	s_barrier
.LBB3_3:
	v_lshl_add_u64 v[156:157], v[108:109], 0, v[96:97]
	v_readfirstlane_b32 s0, v122
	v_add_u32_e32 v160, 0x2000, v122
	v_lshl_add_u64 v[158:159], v[156:157], 0, s[18:19]
	s_mov_b32 m0, s0
	v_readfirstlane_b32 s0, v160
	v_add_u32_e32 v160, 0x4000, v122
	global_load_lds_dwordx4 v[158:159], off
	v_lshl_add_u64 v[158:159], v[156:157], 0, s[2:3]
	s_mov_b32 m0, s0
	v_readfirstlane_b32 s0, v160
	global_load_lds_dwordx4 v[158:159], off
	v_lshl_add_u64 v[158:159], v[156:157], 0, s[8:9]
	s_mov_b32 m0, s0
	v_lshl_add_u64 v[156:157], v[156:157], 0, s[10:11]
	global_load_lds_dwordx4 v[158:159], off
	v_add_u32_e32 v158, 0x6000, v122
	v_add_u32_e32 v160, 0x8000, v122
	v_readfirstlane_b32 s0, v158
	s_mov_b32 m0, s0
	v_readfirstlane_b32 s0, v160
	global_load_lds_dwordx4 v[156:157], off
	v_lshl_add_u64 v[156:157], v[106:107], 0, v[96:97]
	v_lshl_add_u64 v[158:159], v[156:157], 0, s[18:19]
	s_mov_b32 m0, s0
	v_lshl_add_u64 v[156:157], v[156:157], 0, s[2:3]
	global_load_lds_dwordx4 v[158:159], off
	v_add_u32_e32 v158, 0xa000, v122
	ds_read_b128 v[160:163], v123 offset:4096
	v_readfirstlane_b32 s0, v158
	s_mov_b32 m0, s0
	v_readfirstlane_b32 s0, v155
	global_load_lds_dwordx4 v[156:157], off
	v_lshl_add_u64 v[156:157], v[104:105], 0, v[96:97]
	s_mov_b32 m0, s0
	ds_read_b128 v[164:167], v124 offset:32768
	global_load_lds_dwordx4 v[156:157], off
	global_load_dword v202, v[200:201], off
	v_lshl_add_u64 v[200:201], v[200:201], 0, s[40:41]
	ds_read_b128 v[156:159], v123
	ds_read_b128 v[168:171], v124 offset:36864
	ds_read_b128 v[172:175], v125
	s_waitcnt lgkmcnt(0)
	v_mfma_f32_32x32x16_f16 v[80:95], v[156:159], v[164:167], v[80:95]
	ds_read_b128 v[176:179], v126
	v_mfma_f32_32x32x16_f16 v[64:79], v[156:159], v[168:171], v[64:79]
	ds_read_b128 v[180:183], v126 offset:4096
	v_mfma_f32_32x32x16_f16 v[48:63], v[160:163], v[164:167], v[48:63]
	ds_read_b128 v[164:167], v127 offset:32768
	v_mfma_f32_32x32x16_f16 v[32:47], v[160:163], v[168:171], v[32:47]
	ds_read_b128 v[168:171], v127 offset:36864
	v_mfma_f32_32x32x16_f16 v[16:31], v[172:175], v[156:159], v[16:31]
	ds_read_b128 v[156:159], v128
	s_waitcnt lgkmcnt(0)
	v_mfma_f32_32x32x16_f16 v[80:95], v[176:179], v[164:167], v[80:95]
	ds_read_b128 v[184:187], v129
	v_mfma_f32_32x32x16_f16 v[64:79], v[176:179], v[168:171], v[64:79]
	ds_read_b128 v[188:191], v129 offset:4096
	v_mfma_f32_32x32x16_f16 v[48:63], v[180:183], v[164:167], v[48:63]
	ds_read_b128 v[164:167], v130 offset:32768
	v_mfma_f32_32x32x16_f16 v[32:47], v[180:183], v[168:171], v[32:47]
	ds_read_b128 v[168:171], v130 offset:36864
	v_mfma_f32_32x32x16_f16 v[16:31], v[156:159], v[176:179], v[16:31]
	ds_read_b128 v[176:179], v131
	s_waitcnt lgkmcnt(0)
	v_mfma_f32_32x32x16_f16 v[80:95], v[184:187], v[164:167], v[80:95]
	ds_read_b128 v[192:195], v132
	v_mfma_f32_32x32x16_f16 v[64:79], v[184:187], v[168:171], v[64:79]
	ds_read_b128 v[196:199], v132 offset:4096
	v_mfma_f32_32x32x16_f16 v[48:63], v[188:191], v[164:167], v[48:63]
	ds_read_b128 v[164:167], v133 offset:32768
	v_mfma_f32_32x32x16_f16 v[32:47], v[188:191], v[168:171], v[32:47]
	ds_read_b128 v[168:171], v133 offset:36864
	v_mfma_f32_32x32x16_f16 v[16:31], v[176:179], v[184:187], v[16:31]
	ds_read_b128 v[184:187], v134
	s_add_i32 s27, s26, 2
	s_cmp_lt_u32 s26, 30
	s_cselect_b32 s0, s25, 0x7c0
	v_readfirstlane_b32 s30, v115
	s_lshl_b64 s[28:29], s[0:1], 1
	v_readfirstlane_b32 s31, v116
	v_mfma_f32_32x32x16_f16 v[0:15], v[172:175], v[160:163], v[0:15]
	v_lshl_add_u64 v[160:161], v[100:101], 0, s[28:29]
	s_mov_b32 m0, s30
	s_waitcnt vmcnt(1)
	s_waitcnt vmcnt(1) lgkmcnt(0)
	s_barrier
	v_readfirstlane_b32 s33, v117
	v_mfma_f32_32x32x16_f16 v[80:95], v[192:195], v[164:167], v[80:95]
	global_load_lds_dwordx4 v[160:161], off
	s_mov_b32 m0, s31
	v_readfirstlane_b32 s34, v118
	v_readfirstlane_b32 s35, v119
	v_readfirstlane_b32 s36, v120
	v_lshl_add_u64 v[162:163], v[98:99], 0, s[28:29]
	v_mfma_f32_32x32x16_f16 v[48:63], v[196:199], v[164:167], v[48:63]
	v_lshl_add_u64 v[166:167], v[160:161], 0, s[12:13]
	global_load_lds_dwordx4 v[166:167], off
	s_mov_b32 m0, s33
	v_readfirstlane_b32 s37, v121
	v_lshl_add_u64 v[164:165], v[102:103], 0, s[28:29]
	s_addk_i32 s25, 0x80
	v_mfma_f32_32x32x16_f16 v[64:79], v[192:195], v[168:171], v[64:79]
	s_cmp_gt_u32 s26, 29
	v_mfma_f32_32x32x16_f16 v[32:47], v[196:199], v[168:171], v[32:47]
	v_lshl_add_u64 v[168:169], v[160:161], 0, s[14:15]
	v_lshl_add_u64 v[160:161], v[160:161], 0, s[16:17]
	global_load_lds_dwordx4 v[168:169], off
	s_mov_b32 m0, s34
	v_lshl_add_u64 v[170:171], v[162:163], 0, s[12:13]
	global_load_lds_dwordx4 v[160:161], off
	s_mov_b32 m0, s35
	v_mfma_f32_32x32x16_f16 v[0:15], v[156:159], v[180:183], v[0:15]
	global_load_lds_dwordx4 v[162:163], off
	s_mov_b32 m0, s36
	ds_read_b128 v[156:159], v137
	global_load_lds_dwordx4 v[170:171], off
	s_mov_b32 m0, s37
	v_mfma_f32_32x32x16_f16 v[0:15], v[176:179], v[188:191], v[0:15]
	global_load_lds_dwordx4 v[164:165], off
	global_load_dword v202, v[200:201], off
	v_lshl_add_u64 v[200:201], v[200:201], 0, s[40:41]
	ds_read_b128 v[160:163], v138
	ds_read_b128 v[164:167], v139
	ds_read_b128 v[168:171], v135
	ds_read_b128 v[172:175], v136
	v_mfma_f32_32x32x16_f16 v[16:31], v[184:187], v[192:195], v[16:31]
	v_mfma_f32_32x32x16_f16 v[0:15], v[184:187], v[196:199], v[0:15]
	s_waitcnt lgkmcnt(0)
	v_mfma_f32_32x32x16_f16 v[80:95], v[168:171], v[156:159], v[80:95]
	ds_read_b128 v[176:179], v140
	v_mfma_f32_32x32x16_f16 v[64:79], v[168:171], v[160:163], v[64:79]
	ds_read_b128 v[180:183], v141
	v_mfma_f32_32x32x16_f16 v[48:63], v[172:175], v[156:159], v[48:63]
	ds_read_b128 v[156:159], v142
	v_mfma_f32_32x32x16_f16 v[32:47], v[172:175], v[160:163], v[32:47]
	ds_read_b128 v[160:163], v143
	v_mfma_f32_32x32x16_f16 v[16:31], v[164:167], v[168:171], v[16:31]
	ds_read_b128 v[168:171], v144
	v_mfma_f32_32x32x16_f16 v[0:15], v[164:167], v[172:175], v[0:15]
	s_waitcnt lgkmcnt(0)
	v_mfma_f32_32x32x16_f16 v[80:95], v[176:179], v[156:159], v[80:95]
	ds_read_b128 v[164:167], v145
	v_mfma_f32_32x32x16_f16 v[64:79], v[176:179], v[160:163], v[64:79]
	ds_read_b128 v[172:175], v146
	v_mfma_f32_32x32x16_f16 v[48:63], v[180:183], v[156:159], v[48:63]
	ds_read_b128 v[156:159], v147
	v_mfma_f32_32x32x16_f16 v[32:47], v[180:183], v[160:163], v[32:47]
	ds_read_b128 v[160:163], v148
	v_mfma_f32_32x32x16_f16 v[16:31], v[168:171], v[176:179], v[16:31]
	ds_read_b128 v[176:179], v149
	v_mfma_f32_32x32x16_f16 v[0:15], v[168:171], v[180:183], v[0:15]
	s_waitcnt lgkmcnt(0)
	v_mfma_f32_32x32x16_f16 v[80:95], v[164:167], v[156:159], v[80:95]
	ds_read_b128 v[168:171], v150
	v_mfma_f32_32x32x16_f16 v[64:79], v[164:167], v[160:163], v[64:79]
	ds_read_b128 v[180:183], v151
	v_mfma_f32_32x32x16_f16 v[48:63], v[172:175], v[156:159], v[48:63]
	ds_read_b128 v[156:159], v152
	v_mfma_f32_32x32x16_f16 v[32:47], v[172:175], v[160:163], v[32:47]
	ds_read_b128 v[160:163], v153
	v_mfma_f32_32x32x16_f16 v[16:31], v[176:179], v[164:167], v[16:31]
	ds_read_b128 v[164:167], v154
	v_mfma_f32_32x32x16_f16 v[0:15], v[176:179], v[172:175], v[0:15]
	s_waitcnt lgkmcnt(0)
	v_mfma_f32_32x32x16_f16 v[80:95], v[168:171], v[156:159], v[80:95]
	s_waitcnt vmcnt(1)
	v_lshl_add_u64 v[104:105], v[104:105], 0, s[20:21]
	v_lshl_add_u64 v[106:107], v[106:107], 0, s[20:21]
	v_lshl_add_u64 v[108:109], v[108:109], 0, s[20:21]
	s_mov_b32 s26, s27
	s_waitcnt vmcnt(1)
	s_barrier
	v_mfma_f32_32x32x16_f16 v[64:79], v[168:171], v[160:163], v[64:79]
	v_mfma_f32_32x32x16_f16 v[48:63], v[180:183], v[156:159], v[48:63]
	v_mfma_f32_32x32x16_f16 v[32:47], v[180:183], v[160:163], v[32:47]
	v_mfma_f32_32x32x16_f16 v[16:31], v[164:167], v[168:171], v[16:31]
	v_mfma_f32_32x32x16_f16 v[0:15], v[164:167], v[180:183], v[0:15]
	s_cbranch_scc0 .LBB3_3
	v_lshlrev_b32_e32 v96, 1, v112
	v_lshl_or_b32 v96, s23, 2, v96
	v_ashrrev_i32_e32 v97, 31, v96
	v_add_u32_e32 v102, s24, v114
	v_lshlrev_b32_e32 v103, 2, v113
	v_lshlrev_b64 v[96:97], 18, v[96:97]
	v_lshl_add_u64 v[96:97], s[4:5], 0, v[96:97]
	v_or_b32_e32 v100, v102, v103
	v_lshlrev_b32_e32 v98, 1, v110
	v_mov_b32_e32 v99, 0
	v_lshl_add_u64 v[96:97], v[96:97], 0, v[98:99]
	s_mov_b32 s0, 0x38800000
	s_cmp_lt_u32 s23, 16
	s_cselect_b32 s0, 0x38b8aa3b, s0
	v_lshlrev_b32_e32 v98, 7, v100
	v_lshl_add_u64 v[100:101], v[96:97], 0, v[98:99]
	v_fma_mixlo_f16 v64, v64, s0, 0
	global_store_short v[100:101], v64, off offset:64
	v_fma_mixlo_f16 v64, v65, s0, 0
	global_store_short v[100:101], v64, off offset:192
	v_fma_mixlo_f16 v64, v66, s0, 0
	global_store_short v[100:101], v64, off offset:320
	v_fma_mixlo_f16 v64, v67, s0, 0
	global_store_short v[100:101], v64, off offset:448
	v_fma_mixlo_f16 v64, v68, s0, 0
	global_store_short v[100:101], v64, off offset:1088
	v_fma_mixlo_f16 v64, v69, s0, 0
	global_store_short v[100:101], v64, off offset:1216
	v_fma_mixlo_f16 v64, v70, s0, 0
	global_store_short v[100:101], v64, off offset:1344
	v_fma_mixlo_f16 v64, v71, s0, 0
	global_store_short v[100:101], v64, off offset:1472
	v_fma_mixlo_f16 v64, v72, s0, 0
	global_store_short v[100:101], v64, off offset:2112
	v_fma_mixlo_f16 v64, v73, s0, 0
	global_store_short v[100:101], v64, off offset:2240
	v_fma_mixlo_f16 v64, v74, s0, 0
	global_store_short v[100:101], v64, off offset:2368
	v_fma_mixlo_f16 v64, v75, s0, 0
	global_store_short v[100:101], v64, off offset:2496
	v_fma_mixlo_f16 v64, v76, s0, 0
	global_store_short v[100:101], v64, off offset:3136
	v_fma_mixlo_f16 v64, v77, s0, 0
	global_store_short v[100:101], v64, off offset:3264
	v_fma_mixlo_f16 v64, v78, s0, 0
	global_store_short v[100:101], v64, off offset:3392
	v_fma_mixlo_f16 v64, v79, s0, 0
	global_store_short v[100:101], v64, off offset:3520
	v_or_b32_e32 v64, 0x1000, v98
	v_mov_b32_e32 v65, v99
	v_fma_mixlo_f16 v48, v48, s0, 0
	v_lshl_add_u64 v[66:67], v[96:97], 0, v[64:65]
	global_store_short v[66:67], v48, off
	v_fma_mixlo_f16 v68, v49, s0, 0
	v_or_b32_e32 v48, 0x1080, v98
	v_mov_b32_e32 v49, v99
	v_lshl_add_u64 v[66:67], v[96:97], 0, v[48:49]
	global_store_short v[66:67], v68, off
	v_or_b32_e32 v66, 0x1100, v98
	v_mov_b32_e32 v67, v99
	v_fma_mixlo_f16 v50, v50, s0, 0
	v_lshl_add_u64 v[68:69], v[96:97], 0, v[66:67]
	global_store_short v[68:69], v50, off
	v_fma_mixlo_f16 v70, v51, s0, 0
	v_or_b32_e32 v50, 0x1180, v98
	v_mov_b32_e32 v51, v99
	v_lshl_add_u64 v[68:69], v[96:97], 0, v[50:51]
	global_store_short v[68:69], v70, off
	v_or_b32_e32 v68, 0x1400, v98
	v_mov_b32_e32 v69, v99
	v_fma_mixlo_f16 v52, v52, s0, 0
	v_lshl_add_u64 v[70:71], v[96:97], 0, v[68:69]
	global_store_short v[70:71], v52, off
	v_fma_mixlo_f16 v72, v53, s0, 0
	v_or_b32_e32 v52, 0x1480, v98
	v_mov_b32_e32 v53, v99
	v_lshl_add_u64 v[70:71], v[96:97], 0, v[52:53]
	global_store_short v[70:71], v72, off
	v_or_b32_e32 v70, 0x1500, v98
	v_mov_b32_e32 v71, v99
	v_fma_mixlo_f16 v54, v54, s0, 0
	v_lshl_add_u64 v[72:73], v[96:97], 0, v[70:71]
	v_fma_mixlo_f16 v80, v80, s0, 0
	global_store_short v[72:73], v54, off
	v_fma_mixlo_f16 v74, v55, s0, 0
	v_or_b32_e32 v54, 0x1580, v98
	v_mov_b32_e32 v55, v99
	global_store_short v[100:101], v80, off
	v_fma_mixlo_f16 v80, v81, s0, 0
	v_lshl_add_u64 v[72:73], v[96:97], 0, v[54:55]
	global_store_short v[100:101], v80, off offset:128
	v_fma_mixlo_f16 v80, v82, s0, 0
	global_store_short v[72:73], v74, off
	v_or_b32_e32 v72, 0x1800, v98
	v_mov_b32_e32 v73, v99
	global_store_short v[100:101], v80, off offset:256
	v_fma_mixlo_f16 v80, v83, s0, 0
	v_fma_mixlo_f16 v56, v56, s0, 0
	v_lshl_add_u64 v[74:75], v[96:97], 0, v[72:73]
	global_store_short v[100:101], v80, off offset:384
	v_fma_mixlo_f16 v80, v84, s0, 0
	global_store_short v[74:75], v56, off
	v_fma_mixlo_f16 v76, v57, s0, 0
	v_or_b32_e32 v56, 0x1880, v98
	v_mov_b32_e32 v57, v99
	global_store_short v[100:101], v80, off offset:1024
	v_fma_mixlo_f16 v80, v85, s0, 0
	v_lshl_add_u64 v[74:75], v[96:97], 0, v[56:57]
	global_store_short v[100:101], v80, off offset:1152
	v_fma_mixlo_f16 v80, v86, s0, 0
	global_store_short v[74:75], v76, off
	v_or_b32_e32 v74, 0x1900, v98
	v_mov_b32_e32 v75, v99
	global_store_short v[100:101], v80, off offset:1280
	v_fma_mixlo_f16 v80, v87, s0, 0
	v_fma_mixlo_f16 v58, v58, s0, 0
	v_lshl_add_u64 v[76:77], v[96:97], 0, v[74:75]
	global_store_short v[100:101], v80, off offset:1408
	v_fma_mixlo_f16 v80, v88, s0, 0
	global_store_short v[76:77], v58, off
	v_fma_mixlo_f16 v78, v59, s0, 0
	v_or_b32_e32 v58, 0x1980, v98
	v_mov_b32_e32 v59, v99
	global_store_short v[100:101], v80, off offset:2048
	v_fma_mixlo_f16 v80, v89, s0, 0
	v_lshl_add_u64 v[76:77], v[96:97], 0, v[58:59]
	global_store_short v[100:101], v80, off offset:2176
	v_fma_mixlo_f16 v80, v90, s0, 0
	global_store_short v[76:77], v78, off
	v_or_b32_e32 v76, 0x1c00, v98
	v_mov_b32_e32 v77, v99
	global_store_short v[100:101], v80, off offset:2304
	v_fma_mixlo_f16 v80, v91, s0, 0
	v_fma_mixlo_f16 v60, v60, s0, 0
	v_lshl_add_u64 v[78:79], v[96:97], 0, v[76:77]
	global_store_short v[100:101], v80, off offset:2432
	v_fma_mixlo_f16 v80, v92, s0, 0
	global_store_short v[78:79], v60, off
	v_fma_mixlo_f16 v82, v61, s0, 0
	v_or_b32_e32 v60, 0x1c80, v98
	v_mov_b32_e32 v61, v99
	global_store_short v[100:101], v80, off offset:3072
	v_fma_mixlo_f16 v80, v93, s0, 0
	v_lshl_add_u64 v[78:79], v[96:97], 0, v[60:61]
	global_store_short v[100:101], v80, off offset:3200
	v_fma_mixlo_f16 v80, v94, s0, 0
	global_store_short v[78:79], v82, off
	v_or_b32_e32 v78, 0x1d00, v98
	v_mov_b32_e32 v79, v99
	global_store_short v[100:101], v80, off offset:3328
	v_fma_mixlo_f16 v80, v95, s0, 0
	v_fma_mixlo_f16 v62, v62, s0, 0
	v_lshl_add_u64 v[82:83], v[96:97], 0, v[78:79]
	v_or_b32_e32 v98, 0x1d80, v98
	global_store_short v[100:101], v80, off offset:3456
	v_lshl_add_u64 v[80:81], v[96:97], 0, 64
	global_store_short v[82:83], v62, off
	v_fma_mixlo_f16 v82, v63, s0, 0
	v_lshl_add_u64 v[62:63], v[96:97], 0, v[98:99]
	global_store_short v[62:63], v82, off
	v_fma_mixlo_f16 v32, v32, s0, 0
	v_lshl_add_u64 v[62:63], v[80:81], 0, v[64:65]
	global_store_short v[62:63], v32, off
	v_fma_mixlo_f16 v62, v33, s0, 0
	v_lshl_add_u64 v[32:33], v[80:81], 0, v[48:49]
	global_store_short v[32:33], v62, off
	v_fma_mixlo_f16 v34, v34, s0, 0
	v_lshl_add_u64 v[32:33], v[80:81], 0, v[66:67]
	global_store_short v[32:33], v34, off
	v_fma_mixlo_f16 v34, v35, s0, 0
	v_lshl_add_u64 v[32:33], v[80:81], 0, v[50:51]
	global_store_short v[32:33], v34, off
	v_fma_mixlo_f16 v34, v36, s0, 0
	v_lshl_add_u64 v[32:33], v[80:81], 0, v[68:69]
	global_store_short v[32:33], v34, off
	v_fma_mixlo_f16 v34, v37, s0, 0
	v_lshl_add_u64 v[32:33], v[80:81], 0, v[52:53]
	global_store_short v[32:33], v34, off
	v_fma_mixlo_f16 v34, v38, s0, 0
	v_lshl_add_u64 v[32:33], v[80:81], 0, v[70:71]
	global_store_short v[32:33], v34, off
	v_fma_mixlo_f16 v34, v39, s0, 0
	v_lshl_add_u64 v[32:33], v[80:81], 0, v[54:55]
	global_store_short v[32:33], v34, off
	v_fma_mixlo_f16 v34, v40, s0, 0
	v_lshl_add_u64 v[32:33], v[80:81], 0, v[72:73]
	global_store_short v[32:33], v34, off
	v_fma_mixlo_f16 v34, v41, s0, 0
	v_lshl_add_u64 v[32:33], v[80:81], 0, v[56:57]
	global_store_short v[32:33], v34, off
	v_fma_mixlo_f16 v34, v42, s0, 0
	v_lshl_add_u64 v[32:33], v[80:81], 0, v[74:75]
	global_store_short v[32:33], v34, off
	v_fma_mixlo_f16 v34, v43, s0, 0
	v_lshl_add_u64 v[32:33], v[80:81], 0, v[58:59]
	global_store_short v[32:33], v34, off
	v_fma_mixlo_f16 v34, v44, s0, 0
	v_lshl_add_u64 v[32:33], v[80:81], 0, v[76:77]
	global_store_short v[32:33], v34, off
	v_fma_mixlo_f16 v34, v45, s0, 0
	v_lshl_add_u64 v[32:33], v[80:81], 0, v[60:61]
	global_store_short v[32:33], v34, off
	v_fma_mixlo_f16 v34, v46, s0, 0
	v_lshl_add_u64 v[32:33], v[80:81], 0, v[78:79]
	global_store_short v[32:33], v34, off
	v_fma_mixlo_f16 v34, v47, s0, 0
	v_lshl_add_u64 v[32:33], v[80:81], 0, v[98:99]
	global_store_short v[32:33], v34, off
	v_or3_b32 v32, v103, v111, s22
	v_or_b32_e32 v33, v102, v110
	v_lshlrev_b32_e32 v98, 1, v33
	v_ashrrev_i32_e32 v33, 31, v32
	v_lshl_add_u64 v[34:35], s[6:7], 0, v[98:99]
	s_mov_b32 s0, 0x38800000
	v_lshlrev_b64 v[36:37], 12, v[32:33]
	v_fma_mixlo_f16 v16, v16, s0, 0
	v_lshl_add_u64 v[36:37], v[34:35], 0, v[36:37]
	v_or_b32_e32 v38, 2, v32
	global_store_short v[36:37], v16, off
	v_or_b32_e32 v16, 1, v32
	v_ashrrev_i32_e32 v39, 31, v38
	v_fma_mixlo_f16 v33, v17, s0, 0
	v_ashrrev_i32_e32 v17, 31, v16
	v_lshlrev_b64 v[38:39], 12, v[38:39]
	v_lshlrev_b64 v[16:17], 12, v[16:17]
	v_fma_mixlo_f16 v18, v18, s0, 0
	v_lshl_add_u64 v[38:39], v[34:35], 0, v[38:39]
	v_or_b32_e32 v40, 8, v32
	v_lshl_add_u64 v[16:17], v[34:35], 0, v[16:17]
	global_store_short v[38:39], v18, off
	v_or_b32_e32 v18, 3, v32
	v_ashrrev_i32_e32 v41, 31, v40
	global_store_short v[16:17], v33, off
	v_fma_mixlo_f16 v33, v19, s0, 0
	v_ashrrev_i32_e32 v19, 31, v18
	v_lshlrev_b64 v[40:41], 12, v[40:41]
	v_lshlrev_b64 v[18:19], 12, v[18:19]
	v_fma_mixlo_f16 v20, v20, s0, 0
	v_lshl_add_u64 v[40:41], v[34:35], 0, v[40:41]
	v_or_b32_e32 v42, 10, v32
	v_lshl_add_u64 v[18:19], v[34:35], 0, v[18:19]
	global_store_short v[40:41], v20, off
	v_or_b32_e32 v20, 9, v32
	v_ashrrev_i32_e32 v43, 31, v42
	global_store_short v[18:19], v33, off
	v_fma_mixlo_f16 v33, v21, s0, 0
	v_ashrrev_i32_e32 v21, 31, v20
	v_lshlrev_b64 v[42:43], 12, v[42:43]
	v_lshlrev_b64 v[20:21], 12, v[20:21]
	v_fma_mixlo_f16 v22, v22, s0, 0
	v_lshl_add_u64 v[42:43], v[34:35], 0, v[42:43]
	v_or_b32_e32 v44, 16, v32
	v_fma_mixlo_f16 v0, v0, s0, 0
	v_lshl_add_u64 v[20:21], v[34:35], 0, v[20:21]
	global_store_short v[42:43], v22, off
	v_or_b32_e32 v22, 11, v32
	v_ashrrev_i32_e32 v45, 31, v44
	global_store_short v[36:37], v0, off offset:64
	v_fma_mixlo_f16 v0, v1, s0, 0
	global_store_short v[20:21], v33, off
	v_fma_mixlo_f16 v33, v23, s0, 0
	v_ashrrev_i32_e32 v23, 31, v22
	v_lshlrev_b64 v[44:45], 12, v[44:45]
	global_store_short v[16:17], v0, off offset:64
	v_fma_mixlo_f16 v0, v2, s0, 0
	v_lshlrev_b64 v[22:23], 12, v[22:23]
	v_fma_mixlo_f16 v24, v24, s0, 0
	v_lshl_add_u64 v[44:45], v[34:35], 0, v[44:45]
	v_or_b32_e32 v46, 18, v32
	global_store_short v[38:39], v0, off offset:64
	v_fma_mixlo_f16 v0, v3, s0, 0
	v_lshl_add_u64 v[22:23], v[34:35], 0, v[22:23]
	global_store_short v[44:45], v24, off
	v_or_b32_e32 v24, 17, v32
	v_ashrrev_i32_e32 v47, 31, v46
	global_store_short v[18:19], v0, off offset:64
	v_fma_mixlo_f16 v0, v4, s0, 0
	global_store_short v[22:23], v33, off
	v_fma_mixlo_f16 v33, v25, s0, 0
	v_ashrrev_i32_e32 v25, 31, v24
	v_lshlrev_b64 v[46:47], 12, v[46:47]
	global_store_short v[40:41], v0, off offset:64
	v_fma_mixlo_f16 v0, v5, s0, 0
	v_lshlrev_b64 v[24:25], 12, v[24:25]
	v_fma_mixlo_f16 v26, v26, s0, 0
	v_lshl_add_u64 v[46:47], v[34:35], 0, v[46:47]
	v_or_b32_e32 v48, 24, v32
	global_store_short v[20:21], v0, off offset:64
	v_fma_mixlo_f16 v0, v6, s0, 0
	v_lshl_add_u64 v[24:25], v[34:35], 0, v[24:25]
	global_store_short v[46:47], v26, off
	v_or_b32_e32 v26, 19, v32
	v_ashrrev_i32_e32 v49, 31, v48
	global_store_short v[42:43], v0, off offset:64
	v_fma_mixlo_f16 v0, v7, s0, 0
	global_store_short v[24:25], v33, off
	v_fma_mixlo_f16 v33, v27, s0, 0
	v_ashrrev_i32_e32 v27, 31, v26
	v_lshlrev_b64 v[48:49], 12, v[48:49]
	v_or_b32_e32 v50, 26, v32
	global_store_short v[22:23], v0, off offset:64
	v_fma_mixlo_f16 v0, v8, s0, 0
	v_lshlrev_b64 v[26:27], 12, v[26:27]
	v_fma_mixlo_f16 v28, v28, s0, 0
	v_lshl_add_u64 v[48:49], v[34:35], 0, v[48:49]
	v_ashrrev_i32_e32 v51, 31, v50
	global_store_short v[44:45], v0, off offset:64
	v_fma_mixlo_f16 v0, v9, s0, 0
	v_lshl_add_u64 v[26:27], v[34:35], 0, v[26:27]
	global_store_short v[48:49], v28, off
	v_or_b32_e32 v28, 25, v32
	v_lshlrev_b64 v[50:51], 12, v[50:51]
	global_store_short v[24:25], v0, off offset:64
	v_fma_mixlo_f16 v0, v10, s0, 0
	global_store_short v[26:27], v33, off
	v_fma_mixlo_f16 v33, v29, s0, 0
	v_ashrrev_i32_e32 v29, 31, v28
	v_fma_mixlo_f16 v30, v30, s0, 0
	v_lshl_add_u64 v[50:51], v[34:35], 0, v[50:51]
	global_store_short v[46:47], v0, off offset:64
	v_fma_mixlo_f16 v0, v11, s0, 0
	v_lshlrev_b64 v[28:29], 12, v[28:29]
	global_store_short v[50:51], v30, off
	v_or_b32_e32 v30, 27, v32
	global_store_short v[26:27], v0, off offset:64
	v_fma_mixlo_f16 v0, v12, s0, 0
	v_lshl_add_u64 v[28:29], v[34:35], 0, v[28:29]
	v_fma_mixlo_f16 v32, v31, s0, 0
	v_ashrrev_i32_e32 v31, 31, v30
	global_store_short v[48:49], v0, off offset:64
	v_fma_mixlo_f16 v0, v13, s0, 0
	v_lshlrev_b64 v[30:31], 12, v[30:31]
	global_store_short v[28:29], v0, off offset:64
	v_fma_mixlo_f16 v0, v14, s0, 0
	v_lshl_add_u64 v[30:31], v[34:35], 0, v[30:31]
	global_store_short v[50:51], v0, off offset:64
	v_fma_mixlo_f16 v0, v15, s0, 0
	global_store_short v[28:29], v33, off
	global_store_short v[30:31], v32, off
	global_store_short v[30:31], v0, off offset:64
	s_endpgm

	.amdhsa_kernel _Z10qkv_kernelPKDF16_S0_PDF16_S1_
		.amdhsa_group_segment_fixed_size 0
		.amdhsa_private_segment_fixed_size 0
		.amdhsa_kernarg_size 32
		.amdhsa_user_sgpr_count 2
		.amdhsa_user_sgpr_dispatch_ptr 0
		.amdhsa_user_sgpr_queue_ptr 0
		.amdhsa_user_sgpr_kernarg_segment_ptr 1
		.amdhsa_user_sgpr_dispatch_id 0
		.amdhsa_user_sgpr_kernarg_preload_length 0
		.amdhsa_user_sgpr_kernarg_preload_offset 0
		.amdhsa_user_sgpr_private_segment_size 0
		.amdhsa_uses_dynamic_stack 0
		.amdhsa_enable_private_segment 0
		.amdhsa_system_sgpr_workgroup_id_x 1
		.amdhsa_system_sgpr_workgroup_id_y 0
		.amdhsa_system_sgpr_workgroup_id_z 0
		.amdhsa_system_sgpr_workgroup_info 0
		.amdhsa_system_vgpr_workitem_id 0
		.amdhsa_next_free_vgpr 210
		.amdhsa_next_free_sgpr 43
		.amdhsa_accum_offset 212
		.amdhsa_reserve_vcc 1
		.amdhsa_float_round_mode_32 0
		.amdhsa_float_round_mode_16_64 0
		.amdhsa_float_denorm_mode_32 3
		.amdhsa_float_denorm_mode_16_64 3
		.amdhsa_dx10_clamp 1
		.amdhsa_ieee_mode 1
		.amdhsa_fp16_overflow 0
		.amdhsa_tg_split 0
		.amdhsa_exception_fp_ieee_invalid_op 0
		.amdhsa_exception_fp_denorm_src 0
		.amdhsa_exception_fp_ieee_div_zero 0
		.amdhsa_exception_fp_ieee_overflow 0
		.amdhsa_exception_fp_ieee_underflow 0
		.amdhsa_exception_fp_ieee_inexact 0
		.amdhsa_exception_int_div_zero 0
	.end_amdhsa_kernel

amdhsa.kernels:
  - .agpr_count:     0
    .args:
      - .actual_access:  read_only
        .address_space:  global
        .offset:         0
        .size:           8
        .value_kind:     global_buffer
      - .actual_access:  write_only
        .address_space:  global
        .offset:         8
        .size:           8
        .value_kind:     global_buffer
    .group_segment_fixed_size: 0
    .kernarg_segment_align: 8
    .kernarg_segment_size: 16
    .language:       OpenCL C
    .language_version:
      - 2
      - 0
    .max_flat_workgroup_size: 256
    .name:           _Z13conv_x_kernelPKfPDF16_
    .private_segment_fixed_size: 0
    .sgpr_count:     14
    .sgpr_spill_count: 0
    .symbol:         _Z13conv_x_kernelPKfPDF16_.kd
    .uniform_work_group_size: 1
    .uses_dynamic_stack: false
    .vgpr_count:     12
    .vgpr_spill_count: 0
    .wavefront_size: 64
  - .agpr_count:     0
    .args:
      - .actual_access:  read_only
        .address_space:  global
        .offset:         0
        .size:           8
        .value_kind:     global_buffer
      - .actual_access:  read_only
        .address_space:  global
        .offset:         8
        .size:           8
        .value_kind:     global_buffer
      - .actual_access:  read_only
        .address_space:  global
        .offset:         16
        .size:           8
        .value_kind:     global_buffer
      - .actual_access:  read_only
        .address_space:  global
        .offset:         24
        .size:           8
        .value_kind:     global_buffer
      - .actual_access:  write_only
        .address_space:  global
        .offset:         32
        .size:           8
        .value_kind:     global_buffer
      - .actual_access:  write_only
        .address_space:  global
        .offset:         40
        .size:           8
        .value_kind:     global_buffer
      - .actual_access:  read_only
        .address_space:  global
        .offset:         48
        .size:           8
        .value_kind:     global_buffer
      - .actual_access:  write_only
        .address_space:  global
        .offset:         56
        .size:           8
        .value_kind:     global_buffer
    .group_segment_fixed_size: 16640
    .kernarg_segment_align: 8
    .kernarg_segment_size: 64
    .language:       OpenCL C
    .language_version:
      - 2
      - 0
    .max_flat_workgroup_size: 256
    .name:           _Z13conv_w_kernelPKfS0_S0_S0_PDF16_S1_S0_S1_
    .private_segment_fixed_size: 0
    .sgpr_count:     26
    .sgpr_spill_count: 0
    .symbol:         _Z13conv_w_kernelPKfS0_S0_S0_PDF16_S1_S0_S1_.kd
    .uniform_work_group_size: 1
    .uses_dynamic_stack: false
    .vgpr_count:     31
    .vgpr_spill_count: 0
    .wavefront_size: 64
  - .agpr_count:     0
    .args:
      - .actual_access:  read_only
        .address_space:  global
        .offset:         0
        .size:           8
        .value_kind:     global_buffer
      - .actual_access:  read_only
        .address_space:  global
        .offset:         8
        .size:           8
        .value_kind:     global_buffer
      - .actual_access:  write_only
        .address_space:  global
        .offset:         16
        .size:           8
        .value_kind:     global_buffer
    .group_segment_fixed_size: 0
    .kernarg_segment_align: 8
    .kernarg_segment_size: 24
    .language:       OpenCL C
    .language_version:
      - 2
      - 0
    .max_flat_workgroup_size: 512
    .name:           _Z9wo_kernelPKDF16_S0_Pf
    .private_segment_fixed_size: 0
    .sgpr_count:     16
    .sgpr_spill_count: 0
    .symbol:         _Z9wo_kernelPKDF16_S0_Pf.kd
    .uniform_work_group_size: 1
    .uses_dynamic_stack: false
    .vgpr_count:     134
    .vgpr_spill_count: 0
    .wavefront_size: 64
  - .agpr_count:     0
    .args:
      - .address_space:  global
        .offset:         0
        .size:           8
        .value_kind:     global_buffer
      - .address_space:  global
        .offset:         8
        .size:           8
        .value_kind:     global_buffer
      - .actual_access:  write_only
        .address_space:  global
        .offset:         16
        .size:           8
        .value_kind:     global_buffer
      - .actual_access:  write_only
        .address_space:  global
        .offset:         24
        .size:           8
        .value_kind:     global_buffer
    .group_segment_fixed_size: 0
    .kernarg_segment_align: 8
    .kernarg_segment_size: 32
    .language:       OpenCL C
    .language_version:
      - 2
      - 0
    .max_flat_workgroup_size: 512
    .name:           _Z10qkv_kernelPKDF16_S0_PDF16_S1_
    .private_segment_fixed_size: 0
    .sgpr_count:     49
    .sgpr_spill_count: 0
    .symbol:         _Z10qkv_kernelPKDF16_S0_PDF16_S1_.kd
    .uniform_work_group_size: 1
    .uses_dynamic_stack: false
    .vgpr_count:     210
    .vgpr_spill_count: 0
    .wavefront_size: 64
  - .agpr_count:     0
    .args:
      - .actual_access:  read_only
        .address_space:  global
        .offset:         0
        .size:           8
        .value_kind:     global_buffer
      - .actual_access:  read_only
        .address_space:  global
        .offset:         8
        .size:           8
        .value_kind:     global_buffer
      - .actual_access:  read_only
        .address_space:  global
        .offset:         16
        .size:           8
        .value_kind:     global_buffer
      - .actual_access:  read_only
        .address_space:  global
        .offset:         24
        .size:           8
        .value_kind:     global_buffer
      - .actual_access:  read_only
        .address_space:  global
        .offset:         32
        .size:           8
        .value_kind:     global_buffer
      - .actual_access:  read_only
        .address_space:  global
        .offset:         40
        .size:           8
        .value_kind:     global_buffer
      - .actual_access:  read_only
        .address_space:  global
        .offset:         48
        .size:           8
        .value_kind:     global_buffer
      - .actual_access:  write_only
        .address_space:  global
        .offset:         56
        .size:           8
        .value_kind:     global_buffer
      - .actual_access:  write_only
        .address_space:  global
        .offset:         64
        .size:           8
        .value_kind:     global_buffer
      - .actual_access:  write_only
        .address_space:  global
        .offset:         72
        .size:           8
        .value_kind:     global_buffer
    .group_segment_fixed_size: 0
    .kernarg_segment_align: 8
    .kernarg_segment_size: 80
    .language:       OpenCL C
    .language_version:
      - 2
      - 0
    .max_flat_workgroup_size: 512
    .name:           _Z11attn_kernelPKDF16_S0_PKfS2_S2_S2_S2_PfPDF16_S3_
    .private_segment_fixed_size: 0
    .sgpr_count:     44
    .sgpr_spill_count: 0
    .symbol:         _Z11attn_kernelPKDF16_S0_PKfS2_S2_S2_S2_PfPDF16_S3_.kd
    .uniform_work_group_size: 1
    .uses_dynamic_stack: false
    .vgpr_count:     256
    .vgpr_spill_count: 0
    .wavefront_size: 64
